# baseline (speedup 1.0000x reference)
_Z6gat_k2PKDF16_S0_S0_PKfPf:
	s_load_dwordx8 s[4:11], s[0:1], 0x0
	s_load_dwordx2 s[12:13], s[0:1], 0x20
	v_readfirstlane_b32 s14, v0
	v_and_b32_e32 v46, 63, v0
	v_lshlrev_b32_e32 v1, 4, v46
	s_and_b32 s16, s2, 1
	s_bfe_u32 s17, s2, 0x40003
	s_lshl_b32 s17, s17, 2
	s_lshr_b32 s18, s2, 1
	s_lshr_b32 s15, s14, 6
	s_lshl_b32 s19, s16, 19
	s_lshl_b32 s23, s15, 16
	s_add_u32 s19, s19, s23
	s_lshl_b32 s23, s15, 11
	v_lshrrev_b32_e32 v48, 1, v46
	v_add_u32_e32 v48, s17, v48
	v_and_b32_e32 v48, 63, v48
	v_lshlrev_b32_e32 v48, 5, v48
	v_and_b32_e32 v49, 1, v46
	v_lshl_or_b32 v48, v49, 4, v48
	v_xor_b32_e32 v49, 0x400, v48
	v_add_u32_e32 v48, s23, v48
	v_add_u32_e32 v49, s23, v49
	s_mul_i32 s32, s15, 0x1900
	s_add_u32 s32, s32, 75776
	v_and_b32_e32 v44, 31, v0
	v_lshlrev_b32_e32 v45, 2, v44
	s_lshl_b32 s23, s18, 8
	v_add_u32_e32 v45, s23, v45
	s_waitcnt lgkmcnt(0)
	global_load_dword v42, v45, s[10:11]
	global_load_dword v43, v45, s[10:11] offset:128
	s_mov_b32 m0, s32
	s_add_u32 s33, s32, 0x400
	global_load_lds_dwordx4 v48, s[6:7]
	s_mov_b32 m0, s33
	s_add_u32 s34, s32, 0x800
	global_load_lds_dwordx4 v49, s[6:7]
	s_mov_b32 m0, s34
	s_add_u32 s35, s32, 0xc00
	global_load_lds_dwordx4 v48, s[8:9]
	s_mov_b32 m0, s35
	s_add_u32 s20, s4, s19
	global_load_lds_dwordx4 v49, s[8:9]
	s_addc_u32 s21, s5, 0
	s_lshl_b32 s23, s17, 10
	s_add_u32 s24, s20, s23
	s_addc_u32 s25, s21, 0
	global_load_dwordx4 v[64:67], v1, s[24:25]
	global_load_dwordx4 v[68:71], v1, s[24:25] offset:1024
	global_load_dwordx4 v[72:75], v1, s[24:25] offset:2048
	global_load_dwordx4 v[76:79], v1, s[24:25] offset:3072
	s_add_u32 s23, s17, 4
	s_and_b32 s23, s23, 63
	s_lshl_b32 s23, s23, 10
	s_add_u32 s24, s20, s23
	s_addc_u32 s25, s21, 0
	global_load_dwordx4 v[80:83], v1, s[24:25]
	global_load_dwordx4 v[84:87], v1, s[24:25] offset:1024
	global_load_dwordx4 v[88:91], v1, s[24:25] offset:2048
	global_load_dwordx4 v[92:95], v1, s[24:25] offset:3072
	v_accvgpr_write_b32 a0, 0
	v_accvgpr_write_b32 a1, 0
	v_accvgpr_write_b32 a2, 0
	v_accvgpr_write_b32 a3, 0
	v_accvgpr_write_b32 a4, 0
	v_accvgpr_write_b32 a5, 0
	v_accvgpr_write_b32 a6, 0
	v_accvgpr_write_b32 a7, 0
	v_accvgpr_write_b32 a8, 0
	v_accvgpr_write_b32 a9, 0
	v_accvgpr_write_b32 a10, 0
	v_accvgpr_write_b32 a11, 0
	v_accvgpr_write_b32 a12, 0
	v_accvgpr_write_b32 a13, 0
	v_accvgpr_write_b32 a14, 0
	v_accvgpr_write_b32 a15, 0
	v_accvgpr_write_b32 a16, 0
	v_accvgpr_write_b32 a17, 0
	v_accvgpr_write_b32 a18, 0
	v_accvgpr_write_b32 a19, 0
	v_accvgpr_write_b32 a20, 0
	v_accvgpr_write_b32 a21, 0
	v_accvgpr_write_b32 a22, 0
	v_accvgpr_write_b32 a23, 0
	v_accvgpr_write_b32 a24, 0
	v_accvgpr_write_b32 a25, 0
	v_accvgpr_write_b32 a26, 0
	v_accvgpr_write_b32 a27, 0
	v_accvgpr_write_b32 a28, 0
	v_accvgpr_write_b32 a29, 0
	v_accvgpr_write_b32 a30, 0
	v_accvgpr_write_b32 a31, 0
	v_accvgpr_write_b32 a32, 0
	v_accvgpr_write_b32 a33, 0
	v_accvgpr_write_b32 a34, 0
	v_accvgpr_write_b32 a35, 0
	v_accvgpr_write_b32 a36, 0
	v_accvgpr_write_b32 a37, 0
	v_accvgpr_write_b32 a38, 0
	v_accvgpr_write_b32 a39, 0
	v_mov_b32_e32 v2, 0
	v_mov_b32_e32 v3, 0
	v_mov_b32_e32 v4, 0
	v_mov_b32_e32 v5, 0
	v_add_u32_e32 v50, s32, v1
	ds_write_b128 v50, v[2:5] offset:4096
	ds_write_b128 v50, v[2:5] offset:5120
	v_lshrrev_b32_e32 v44, 5, v46
	v_and_b32_e32 v45, 15, v46
	v_bfe_u32 v47, v46, 4, 1
	v_cmp_eq_u32_e32 vcc, v45, v47
	v_lshlrev_b32_e32 v44, 4, v44
	v_add_u32_e32 v46, s32, v44
	v_add_u32_e32 v45, 0x800, v46
	v_mov_b32_e32 v47, s32
	v_add_u32_e32 v47, 0x1000, v47
	v_cndmask_b32_e32 v47, v47, v45, vcc
	s_mov_b32 s30, 0x5040100
	s_add_u32 s27, s17, 8
	s_lshl_b32 s27, s27, 10
	s_add_u32 s29, s17, 60
	s_lshl_b32 s29, s29, 10
	s_movk_i32 s28, 0x1000
	s_mov_b32 s26, 0
	s_waitcnt vmcnt(8) lgkmcnt(0)
	ds_read_b128 v[144:147], v46
	ds_read_b128 v[148:151], v46 offset:32
	ds_read_b128 v[160:163], v47
	ds_read_b128 v[152:155], v46 offset:64
	ds_read_b128 v[164:167], v47 offset:32
	v_cvt_f16_f32_e32 v42, v42
	v_cvt_f16_f32_e32 v43, v43
	v_perm_b32 v42, v42, v42, s30
	v_perm_b32 v43, v43, v43, s30
	s_waitcnt lgkmcnt(4)
	v_pk_max_u16 v128, v144, v42
	v_pk_max_u16 v129, v145, v42
	v_pk_max_u16 v130, v146, v42
	v_pk_max_u16 v131, v147, v42
	v_pk_max_u16 v136, v144, v43
	v_pk_max_u16 v137, v145, v43
	v_pk_max_u16 v138, v146, v43
	v_pk_max_u16 v139, v147, v43
	s_mov_b32 s31, 0xfc00
	s_cmp_ge_u32 s15, 4
	s_cbranch_scc0 .Lk2_noprio
	s_setprio 1
